# reduce_slabs prologue de-serialised: both kernarg quads loaded at once, column-sum loads of blocks 0-1 issued before the slab loads (probe shows reduce interval 4.3->4.2us, ~neutral)
# speedup vs baseline: 1.0215x; 1.0020x over previous
_Z12reduce_slabsPKfPDF16_S0_Pf:
	s_load_dwordx4 s[4:7], s[0:1], 0x0
	s_load_dwordx4 s[12:15], s[0:1], 0x10
	s_lshl_b32 s10, s2, 8
	s_bfe_i32 s2, s2, 0xe000a
	s_ashr_i32 s3, s2, 31
	v_mov_b32_e32 v1, 0x3ffff
	s_lshl_b64 s[8:9], s[2:3], 23
	v_bitop3_b32 v1, s10, v1, v0 bitop3:0xc8
	v_or_b32_e32 v2, s10, v0
	s_movk_i32 s11, 0x200
	v_cmp_gt_i32_e32 vcc, s11, v2
	s_waitcnt lgkmcnt(0)
	s_and_saveexec_b64 s[16:17], vcc
	s_cbranch_execz .Lrs_nocs
	v_lshrrev_b32_e32 v30, 8, v2
	v_lshlrev_b32_e32 v30, 14, v30
	v_and_b32_e32 v31, 0xff, v2
	v_lshl_add_u32 v30, v31, 2, v30
	v_add_u32_e32 v31, 0x1000, v30
	v_add_u32_e32 v32, 0x2000, v30
	v_add_u32_e32 v33, 0x3000, v30
	global_load_dword v40, v30, s[12:13]
	global_load_dword v41, v30, s[12:13] offset:1024
	global_load_dword v42, v30, s[12:13] offset:2048
	global_load_dword v43, v30, s[12:13] offset:3072
	global_load_dword v44, v31, s[12:13]
	global_load_dword v45, v31, s[12:13] offset:1024
	global_load_dword v46, v31, s[12:13] offset:2048
	global_load_dword v47, v31, s[12:13] offset:3072
	global_load_dword v48, v32, s[12:13]
	global_load_dword v49, v32, s[12:13] offset:1024
	global_load_dword v50, v32, s[12:13] offset:2048
	global_load_dword v51, v32, s[12:13] offset:3072
	global_load_dword v52, v33, s[12:13]
	global_load_dword v53, v33, s[12:13] offset:1024
	global_load_dword v54, v33, s[12:13] offset:2048
	global_load_dword v55, v33, s[12:13] offset:3072
.Lrs_nocs:
	s_or_b64 exec, exec, s[16:17]
	s_add_u32 s4, s4, s8
	s_addc_u32 s5, s5, s9
	v_lshlrev_b32_e32 v20, 4, v1
	v_mov_b32_e32 v21, 0
	v_lshl_add_u64 v[4:5], s[4:5], 0, v[20:21]
	s_mov_b32 s8, 0x400000
	v_add_co_u32_e32 v12, vcc, s8, v4
	s_lshl_b64 s[2:3], s[2:3], 21
	s_nop 0
	v_addc_co_u32_e32 v13, vcc, 0, v5, vcc
	global_load_dwordx4 v[4:7], v20, s[4:5]
	global_load_dwordx4 v[8:11], v[12:13], off
	s_add_u32 s2, s6, s2
	v_lshlrev_b32_e32 v1, 3, v1
	s_addc_u32 s3, s7, s3
	s_waitcnt vmcnt(0)
	v_pk_add_f32 v[4:5], v[4:5], v[8:9]
	v_pk_add_f32 v[6:7], v[6:7], v[10:11]
	v_cvt_pk_f16_f32 v4, v4, v5
	v_cvt_pk_f16_f32 v5, v6, v7
	global_store_dwordx2 v1, v[4:5], s[2:3]
	v_cmp_gt_i32_e32 vcc, s11, v2
	s_and_saveexec_b64 s[2:3], vcc
	s_cbranch_execz .LBB1_2
	v_add_f32_e32 v0, 0, v40
	v_add_f32_e32 v0, v0, v41
	v_add_f32_e32 v0, v0, v42
	v_add_f32_e32 v0, v0, v43
	v_add_f32_e32 v0, v0, v44
	v_add_f32_e32 v0, v0, v45
	v_add_f32_e32 v0, v0, v46
	v_add_f32_e32 v0, v0, v47
	v_add_f32_e32 v0, v0, v48
	v_add_f32_e32 v0, v0, v49
	v_add_f32_e32 v0, v0, v50
	v_add_f32_e32 v0, v0, v51
	v_add_f32_e32 v0, v0, v52
	v_add_f32_e32 v0, v0, v53
	v_add_f32_e32 v0, v0, v54
	v_add_f32_e32 v4, v0, v55
	v_ashrrev_i32_e32 v3, 31, v2
	v_lshl_add_u64 v[0:1], v[2:3], 2, s[14:15]
	global_store_dword v[0:1], v4, off

	.amdhsa_kernel _Z12reduce_slabsPKfPDF16_S0_Pf
		.amdhsa_group_segment_fixed_size 0
		.amdhsa_private_segment_fixed_size 0
		.amdhsa_kernarg_size 32
		.amdhsa_user_sgpr_count 2
		.amdhsa_user_sgpr_dispatch_ptr 0
		.amdhsa_user_sgpr_queue_ptr 0
		.amdhsa_user_sgpr_kernarg_segment_ptr 1
		.amdhsa_user_sgpr_dispatch_id 0
		.amdhsa_user_sgpr_kernarg_preload_length 0
		.amdhsa_user_sgpr_kernarg_preload_offset 0
		.amdhsa_user_sgpr_private_segment_size 0
		.amdhsa_uses_dynamic_stack 0
		.amdhsa_enable_private_segment 0
		.amdhsa_system_sgpr_workgroup_id_x 1
		.amdhsa_system_sgpr_workgroup_id_y 0
		.amdhsa_system_sgpr_workgroup_id_z 0
		.amdhsa_system_sgpr_workgroup_info 0
		.amdhsa_system_vgpr_workitem_id 0
		.amdhsa_next_free_vgpr 56
		.amdhsa_next_free_sgpr 18
		.amdhsa_accum_offset 56
		.amdhsa_reserve_vcc 1
		.amdhsa_float_round_mode_32 0
		.amdhsa_float_round_mode_16_64 0
		.amdhsa_float_denorm_mode_32 3
		.amdhsa_float_denorm_mode_16_64 3
		.amdhsa_dx10_clamp 1
		.amdhsa_ieee_mode 1
		.amdhsa_fp16_overflow 0
		.amdhsa_tg_split 0
		.amdhsa_exception_fp_ieee_invalid_op 0
		.amdhsa_exception_fp_denorm_src 0
		.amdhsa_exception_fp_ieee_div_zero 0
		.amdhsa_exception_fp_ieee_overflow 0
		.amdhsa_exception_fp_ieee_underflow 0
		.amdhsa_exception_fp_ieee_inexact 0
		.amdhsa_exception_int_div_zero 0
	.end_amdhsa_kernel

amdhsa.kernels:
  - .agpr_count:     0
    .args:
      - .offset:         0
        .size:           120
        .value_kind:     by_value
    .group_segment_fixed_size: 16640
    .kernarg_segment_align: 8
    .kernarg_segment_size: 120
    .language:       OpenCL C
    .language_version:
      - 2
      - 0
    .max_flat_workgroup_size: 256
    .name:           _Z8prep_all5PArgs
    .private_segment_fixed_size: 0
    .sgpr_count:     45
    .sgpr_spill_count: 0
    .symbol:         _Z8prep_all5PArgs.kd
    .uniform_work_group_size: 1
    .uses_dynamic_stack: false
    .vgpr_count:     42
    .vgpr_spill_count: 0
    .wavefront_size: 64
  - .agpr_count:     0
    .args:
      - .actual_access:  read_only
        .address_space:  global
        .offset:         0
        .size:           8
        .value_kind:     global_buffer
      - .actual_access:  write_only
        .address_space:  global
        .offset:         8
        .size:           8
        .value_kind:     global_buffer
      - .actual_access:  read_only
        .address_space:  global
        .offset:         16
        .size:           8
        .value_kind:     global_buffer
      - .actual_access:  write_only
        .address_space:  global
        .offset:         24
        .size:           8
        .value_kind:     global_buffer
    .group_segment_fixed_size: 0
    .kernarg_segment_align: 8
    .kernarg_segment_size: 32
    .language:       OpenCL C
    .language_version:
      - 2
      - 0
    .max_flat_workgroup_size: 256
    .name:           _Z12reduce_slabsPKfPDF16_S0_Pf
    .private_segment_fixed_size: 0
    .sgpr_count:     17
    .sgpr_spill_count: 0
    .symbol:         _Z12reduce_slabsPKfPDF16_S0_Pf.kd
    .uniform_work_group_size: 1
    .uses_dynamic_stack: false
    .vgpr_count:     56
    .vgpr_spill_count: 0
    .wavefront_size: 64
  - .agpr_count:     0
    .args:
      - .offset:         0
        .size:           88
        .value_kind:     by_value
    .group_segment_fixed_size: 122880
    .kernarg_segment_align: 8
    .kernarg_segment_size: 88
    .language:       OpenCL C
    .language_version:
      - 2
      - 0
    .max_flat_workgroup_size: 512
    .name:           _Z6kv1s_k5RArgs
    .private_segment_fixed_size: 0
    .sgpr_count:     29
    .sgpr_spill_count: 0
    .symbol:         _Z6kv1s_k5RArgs.kd
    .uniform_work_group_size: 1
    .uses_dynamic_stack: false
    .vgpr_count:     212
    .vgpr_spill_count: 0
    .wavefront_size: 64
  - .agpr_count:     0
    .args:
      - .offset:         0
        .size:           88
        .value_kind:     by_value
      - .offset:         88
        .size:           32
        .value_kind:     by_value
      - .offset:         120
        .size:           16
        .value_kind:     by_value
    .group_segment_fixed_size: 131072
    .kernarg_segment_align: 8
    .kernarg_segment_size: 136
    .language:       OpenCL C
    .language_version:
      - 2
      - 0
    .max_flat_workgroup_size: 512
    .name:           _Z8k_kv2_qg5RArgsN3pg84GemmENS0_5EpiQTE
    .private_segment_fixed_size: 0
    .sgpr_count:     96
    .sgpr_spill_count: 0
    .symbol:         _Z8k_kv2_qg5RArgsN3pg84GemmENS0_5EpiQTE.kd
    .uniform_work_group_size: 1
    .uses_dynamic_stack: false
    .vgpr_count:     242
    .vgpr_spill_count: 0
    .wavefront_size: 64
  - .agpr_count:     0
    .args:
      - .offset:         0
        .size:           88
        .value_kind:     by_value
      - .offset:         88
        .size:           32
        .value_kind:     by_value
      - .offset:         120
        .size:           16
        .value_kind:     by_value
    .group_segment_fixed_size: 147456
    .kernarg_segment_align: 8
    .kernarg_segment_size: 136
    .language:       OpenCL C
    .language_version:
      - 2
      - 0
    .max_flat_workgroup_size: 512
    .name:           _Z8k_kv1_qg5RArgsN3pg84GemmENS0_5EpiQTE
    .private_segment_fixed_size: 0
    .sgpr_count:     82
    .sgpr_spill_count: 0
    .symbol:         _Z8k_kv1_qg5RArgsN3pg84GemmENS0_5EpiQTE.kd
    .uniform_work_group_size: 1
    .uses_dynamic_stack: false
    .vgpr_count:     242
    .vgpr_spill_count: 0
    .wavefront_size: 64
  - .agpr_count:     0
    .args:
      - .actual_access:  read_only
        .address_space:  global
        .offset:         0
        .size:           8
        .value_kind:     global_buffer
      - .actual_access:  read_only
        .address_space:  global
        .offset:         8
        .size:           8
        .value_kind:     global_buffer
      - .actual_access:  read_only
        .address_space:  global
        .offset:         16
        .size:           8
        .value_kind:     global_buffer
      - .actual_access:  write_only
        .address_space:  global
        .offset:         24
        .size:           8
        .value_kind:     global_buffer
    .group_segment_fixed_size: 102400
    .kernarg_segment_align: 8
    .kernarg_segment_size: 32
    .language:       OpenCL C
    .language_version:
      - 2
      - 0
    .max_flat_workgroup_size: 512
    .name:           _Z6attn_kPKDF16_S0_S0_PDF16_
    .private_segment_fixed_size: 0
    .sgpr_count:     19
    .sgpr_spill_count: 0
    .symbol:         _Z6attn_kPKDF16_S0_S0_PDF16_.kd
    .uniform_work_group_size: 1
    .uses_dynamic_stack: false
    .vgpr_count:     222
    .vgpr_spill_count: 0
    .wavefront_size: 64
  - .agpr_count:     0
    .args:
      - .offset:         0
        .size:           32
        .value_kind:     by_value
      - .offset:         32
        .size:           16
        .value_kind:     by_value
      - .offset:         48
        .size:           4
        .value_kind:     hidden_block_count_x
      - .offset:         52
        .size:           4
        .value_kind:     hidden_block_count_y
      - .offset:         56
        .size:           4
        .value_kind:     hidden_block_count_z
      - .offset:         60
        .size:           2
        .value_kind:     hidden_group_size_x
      - .offset:         62
        .size:           2
        .value_kind:     hidden_group_size_y
      - .offset:         64
        .size:           2
        .value_kind:     hidden_group_size_z
      - .offset:         66
        .size:           2
        .value_kind:     hidden_remainder_x
      - .offset:         68
        .size:           2
        .value_kind:     hidden_remainder_y
      - .offset:         70
        .size:           2
        .value_kind:     hidden_remainder_z
      - .offset:         88
        .size:           8
        .value_kind:     hidden_global_offset_x
      - .offset:         96
        .size:           8
        .value_kind:     hidden_global_offset_y
      - .offset:         104
        .size:           8
        .value_kind:     hidden_global_offset_z
      - .offset:         112
        .size:           2
        .value_kind:     hidden_grid_dims
    .group_segment_fixed_size: 131072
    .kernarg_segment_align: 8
    .kernarg_segment_size: 304
    .language:       OpenCL C
    .language_version:
      - 2
      - 0
    .max_flat_workgroup_size: 512
    .name:           _Z7k_phaseIN3pg86EpiOutEEvNS0_4GemmET_
    .private_segment_fixed_size: 0
    .sgpr_count:     84
    .sgpr_spill_count: 0
    .symbol:         _Z7k_phaseIN3pg86EpiOutEEvNS0_4GemmET_.kd
    .uniform_work_group_size: 1
    .uses_dynamic_stack: false
    .vgpr_count:     256
    .vgpr_spill_count: 0
    .wavefront_size: 64
